# v51 + k_agg2: fma_mix peephole frees VGPRs, v66/v67 renamed, allocation 80 -> 64 (8 waves per SIMD)
# speedup vs baseline: 1.0258x; 1.0108x over previous
.LBB3_2:
	s_or_b64 exec, exec, s[2:3]
	v_mbcnt_lo_u32_b32 v10, -1, 0
	v_mbcnt_hi_u32_b32 v27, -1, v10
	s_waitcnt vmcnt(1)
	v_cmp_gt_i32_e64 s[2:3], v45, v41
	v_and_or_b32 v9, v27, 64, v9
	v_lshlrev_b32_e32 v47, 2, v9
	s_waitcnt vmcnt(0)
	v_cndmask_b32_e64 v8, v24, v8, s[2:3]
	ds_bpermute_b32 v10, v47, v8
	ds_bpermute_b32 v14, v47, v8 offset:16
	ds_bpermute_b32 v20, v47, v8 offset:48
	v_cndmask_b32_e64 v49, 0, 1.0, s[2:3]
	ds_bpermute_b32 v40, v47, v49
	s_waitcnt lgkmcnt(3)
	v_ashrrev_i32_e32 v11, 31, v10
	v_lshlrev_b64 v[10:11], 7, v[10:11]
	v_lshl_add_u64 v[10:11], v[30:31], 0, v[10:11]
	global_load_dwordx4 v[10:13], v[10:11], off
	s_waitcnt lgkmcnt(2)
	v_ashrrev_i32_e32 v15, 31, v14
	v_lshlrev_b64 v[14:15], 7, v[14:15]
	v_lshl_add_u64 v[14:15], v[30:31], 0, v[14:15]
	global_load_dwordx4 v[14:17], v[14:15], off
	s_waitcnt lgkmcnt(1)
	v_ashrrev_i32_e32 v21, 31, v20
	v_lshlrev_b64 v[22:23], 7, v[20:21]
	v_lshl_add_u64 v[22:23], v[30:31], 0, v[22:23]
	global_load_dwordx4 v[32:35], v[22:23], off
	ds_bpermute_b32 v18, v47, v8 offset:32
	ds_bpermute_b32 v42, v47, v49 offset:16
	ds_bpermute_b32 v44, v47, v49 offset:64
	v_cmp_lt_i32_e64 s[2:3], 32, v45
	s_waitcnt lgkmcnt(2)
	v_ashrrev_i32_e32 v19, 31, v18
	v_lshlrev_b64 v[18:19], 7, v[18:19]
	v_lshl_add_u64 v[18:19], v[30:31], 0, v[18:19]
	global_load_dwordx4 v[18:21], v[18:19], off
	s_waitcnt vmcnt(3)
	v_fma_mix_f32 v6, v40, v10, v6 op_sel_hi:[0,1,0]
	v_fma_mix_f32 v7, v40, v10, v7 op_sel:[0,1,0] op_sel_hi:[0,1,0]
	ds_bpermute_b32 v22, v47, v8 offset:64
	v_fma_mix_f32 v10, v40, v11, v4 op_sel_hi:[0,1,0]
	v_fma_mix_f32 v11, v40, v11, v5 op_sel:[0,1,0] op_sel_hi:[0,1,0]
	ds_bpermute_b32 v4, v47, v8 offset:80
	s_waitcnt lgkmcnt(1)
	v_ashrrev_i32_e32 v23, 31, v22
	v_fma_mix_f32 v36, v40, v12, v2 op_sel_hi:[0,1,0]
	v_fma_mix_f32 v37, v40, v12, v3 op_sel:[0,1,0] op_sel_hi:[0,1,0]
	v_lshlrev_b64 v[2:3], 7, v[22:23]
	v_lshl_add_u64 v[2:3], v[30:31], 0, v[2:3]
	s_waitcnt vmcnt(2)
	v_fma_mix_f32 v22, v40, v13, v0 op_sel_hi:[0,1,0]
	v_fma_mix_f32 v23, v40, v13, v1 op_sel:[0,1,0] op_sel_hi:[0,1,0]
	global_load_dwordx4 v[0:3], v[2:3], off
	ds_bpermute_b32 v12, v47, v8 offset:96
	s_waitcnt lgkmcnt(1)
	v_ashrrev_i32_e32 v5, 31, v4
	v_lshlrev_b64 v[4:5], 7, v[4:5]
	v_lshl_add_u64 v[4:5], v[30:31], 0, v[4:5]
	v_fma_mix_f32 v38, v42, v14, v6 op_sel_hi:[0,1,0]
	v_fma_mix_f32 v39, v42, v14, v7 op_sel:[0,1,0] op_sel_hi:[0,1,0]
	global_load_dwordx4 v[4:7], v[4:5], off
	s_waitcnt lgkmcnt(0)
	v_ashrrev_i32_e32 v13, 31, v12
	v_lshlrev_b64 v[12:13], 7, v[12:13]
	v_lshl_add_u64 v[12:13], v[30:31], 0, v[12:13]
	v_fma_mix_f32 v60, v42, v15, v10 op_sel_hi:[0,1,0]
	v_fma_mix_f32 v61, v42, v15, v11 op_sel:[0,1,0] op_sel_hi:[0,1,0]
	global_load_dwordx4 v[10:13], v[12:13], off
	ds_bpermute_b32 v40, v47, v49 offset:32
	s_waitcnt vmcnt(3)
	v_fma_mix_f32 v50, v42, v16, v36 op_sel_hi:[0,1,0]
	v_fma_mix_f32 v51, v42, v16, v37 op_sel:[0,1,0] op_sel_hi:[0,1,0]
	v_fma_mix_f32 v22, v42, v17, v22 op_sel_hi:[0,1,0]
	v_fma_mix_f32 v23, v42, v17, v23 op_sel:[0,1,0] op_sel_hi:[0,1,0]
	ds_bpermute_b32 v42, v47, v49 offset:48
	s_waitcnt lgkmcnt(1)
	v_fma_mix_f32 v14, v40, v18, v38 op_sel_hi:[0,1,0]
	v_fma_mix_f32 v15, v40, v18, v39 op_sel:[0,1,0] op_sel_hi:[0,1,0]
	s_waitcnt lgkmcnt(0)
	v_fma_mix_f32 v14, v42, v32, v14 op_sel_hi:[0,1,0]
	v_fma_mix_f32 v15, v42, v32, v15 op_sel:[0,1,0] op_sel_hi:[0,1,0]
	v_fma_mix_f32 v18, v40, v19, v60 op_sel_hi:[0,1,0]
	v_fma_mix_f32 v19, v40, v19, v61 op_sel:[0,1,0] op_sel_hi:[0,1,0]
	v_fma_mix_f32 v18, v42, v33, v18 op_sel_hi:[0,1,0]
	v_fma_mix_f32 v19, v42, v33, v19 op_sel:[0,1,0] op_sel_hi:[0,1,0]
	s_waitcnt vmcnt(2)
	v_cvt_f32_f16_e32 v16, v0
	v_cvt_f32_f16_sdwa v17, v0 dst_sel:DWORD dst_unused:UNUSED_PAD src0_sel:WORD_1
	ds_bpermute_b32 v0, v47, v49 offset:80
	v_pk_fma_f32 v[14:15], v[44:45], v[16:17], v[14:15] op_sel_hi:[0,1,1]
	s_waitcnt vmcnt(1)
	v_cvt_f32_f16_e32 v16, v4
	v_cvt_f32_f16_sdwa v17, v4 dst_sel:DWORD dst_unused:UNUSED_PAD src0_sel:WORD_1
	ds_bpermute_b32 v4, v47, v49 offset:96
	v_fma_mix_f32 v18, v44, v1, v18 op_sel_hi:[0,1,0]
	v_fma_mix_f32 v19, v44, v1, v19 op_sel:[0,1,0] op_sel_hi:[0,1,0]
	s_waitcnt lgkmcnt(1)
	v_pk_fma_f32 v[14:15], v[0:1], v[16:17], v[14:15] op_sel_hi:[0,1,1]
	s_waitcnt vmcnt(0)
	v_cvt_f32_f16_e32 v16, v10
	v_cvt_f32_f16_sdwa v17, v10 dst_sel:DWORD dst_unused:UNUSED_PAD src0_sel:WORD_1
	ds_bpermute_b32 v10, v47, v49 offset:112
	s_waitcnt lgkmcnt(1)
	v_pk_fma_f32 v[36:37], v[4:5], v[16:17], v[14:15] op_sel_hi:[0,1,1]
	ds_bpermute_b32 v14, v47, v8 offset:112
	v_fma_mix_f32 v18, v0, v5, v18 op_sel_hi:[0,1,0]
	v_fma_mix_f32 v19, v0, v5, v19 op_sel:[0,1,0] op_sel_hi:[0,1,0]
	s_waitcnt lgkmcnt(0)
	v_ashrrev_i32_e32 v15, 31, v14
	v_lshlrev_b64 v[14:15], 7, v[14:15]
	v_lshl_add_u64 v[14:15], v[30:31], 0, v[14:15]
	global_load_dwordx4 v[14:17], v[14:15], off
	v_fma_mix_f32 v18, v4, v11, v18 op_sel_hi:[0,1,0]
	v_fma_mix_f32 v19, v4, v11, v19 op_sel:[0,1,0] op_sel_hi:[0,1,0]
	s_waitcnt vmcnt(0)
	v_fma_mix_f32 v36, v10, v14, v36 op_sel_hi:[0,1,0]
	v_fma_mix_f32 v37, v10, v14, v37 op_sel:[0,1,0] op_sel_hi:[0,1,0]
	v_fma_mix_f32 v38, v10, v15, v18 op_sel_hi:[0,1,0]
	v_fma_mix_f32 v39, v10, v15, v19 op_sel:[0,1,0] op_sel_hi:[0,1,0]
	v_cvt_f32_f16_e32 v18, v2
	v_cvt_f32_f16_sdwa v19, v2 dst_sel:DWORD dst_unused:UNUSED_PAD src0_sel:WORD_1
	v_fma_mix_f32 v14, v40, v20, v50 op_sel_hi:[0,1,0]
	v_fma_mix_f32 v15, v40, v20, v51 op_sel:[0,1,0] op_sel_hi:[0,1,0]
	v_fma_mix_f32 v14, v42, v34, v14 op_sel_hi:[0,1,0]
	v_fma_mix_f32 v15, v42, v34, v15 op_sel:[0,1,0] op_sel_hi:[0,1,0]
	v_cvt_f32_f16_e32 v2, v3
	v_pk_fma_f32 v[14:15], v[44:45], v[18:19], v[14:15] op_sel_hi:[0,1,1]
	v_cvt_f32_f16_e32 v18, v6
	v_cvt_f32_f16_sdwa v19, v6 dst_sel:DWORD dst_unused:UNUSED_PAD src0_sel:WORD_1
	v_cvt_f32_f16_sdwa v3, v3 dst_sel:DWORD dst_unused:UNUSED_PAD src0_sel:WORD_1
	v_cvt_f32_f16_e32 v6, v7
	v_cvt_f32_f16_sdwa v7, v7 dst_sel:DWORD dst_unused:UNUSED_PAD src0_sel:WORD_1
	v_pk_fma_f32 v[14:15], v[0:1], v[18:19], v[14:15] op_sel_hi:[0,1,1]
	v_cvt_f32_f16_e32 v18, v12
	v_cvt_f32_f16_sdwa v19, v12 dst_sel:DWORD dst_unused:UNUSED_PAD src0_sel:WORD_1
	v_cvt_f32_f16_e32 v12, v13
	v_cvt_f32_f16_sdwa v13, v13 dst_sel:DWORD dst_unused:UNUSED_PAD src0_sel:WORD_1
	v_pk_fma_f32 v[14:15], v[4:5], v[18:19], v[14:15] op_sel_hi:[0,1,1]
	v_cvt_f32_f16_e32 v18, v16
	v_cvt_f32_f16_sdwa v19, v16 dst_sel:DWORD dst_unused:UNUSED_PAD src0_sel:WORD_1
	v_cvt_f32_f16_e32 v16, v17
	v_cvt_f32_f16_sdwa v17, v17 dst_sel:DWORD dst_unused:UNUSED_PAD src0_sel:WORD_1
	v_pk_fma_f32 v[32:33], v[10:11], v[18:19], v[14:15] op_sel_hi:[0,1,1]
	v_fma_mix_f32 v14, v40, v21, v22 op_sel_hi:[0,1,0]
	v_fma_mix_f32 v15, v40, v21, v23 op_sel:[0,1,0] op_sel_hi:[0,1,0]
	v_fma_mix_f32 v14, v42, v35, v14 op_sel_hi:[0,1,0]
	v_fma_mix_f32 v15, v42, v35, v15 op_sel:[0,1,0] op_sel_hi:[0,1,0]
	v_pk_fma_f32 v[2:3], v[44:45], v[2:3], v[14:15] op_sel_hi:[0,1,1]
	v_pk_fma_f32 v[0:1], v[0:1], v[6:7], v[2:3] op_sel_hi:[0,1,1]
	v_pk_fma_f32 v[0:1], v[4:5], v[12:13], v[0:1] op_sel_hi:[0,1,1]
	v_pk_fma_f32 v[34:35], v[10:11], v[16:17], v[0:1] op_sel_hi:[0,1,1]
	s_and_saveexec_b64 s[6:7], s[2:3]
	s_cbranch_execz .LBB3_4
	ds_bpermute_b32 v0, v47, v8 offset:128
	ds_bpermute_b32 v2, v47, v8 offset:144
	ds_bpermute_b32 v4, v47, v8 offset:176
	ds_bpermute_b32 v6, v47, v8 offset:208
	ds_bpermute_b32 v10, v47, v8 offset:224
	s_waitcnt lgkmcnt(4)
	v_ashrrev_i32_e32 v1, 31, v0
	s_waitcnt lgkmcnt(3)
	v_ashrrev_i32_e32 v3, 31, v2
	v_lshlrev_b64 v[0:1], 7, v[0:1]
	v_lshlrev_b64 v[2:3], 7, v[2:3]
	v_lshl_add_u64 v[0:1], v[30:31], 0, v[0:1]
	v_lshl_add_u64 v[2:3], v[30:31], 0, v[2:3]
	global_load_dwordx4 v[52:55], v[0:1], off
	global_load_dwordx4 v[58:61], v[2:3], off
	ds_bpermute_b32 v0, v47, v8 offset:160
	ds_bpermute_b32 v2, v47, v8 offset:192
	s_waitcnt lgkmcnt(4)
	v_ashrrev_i32_e32 v5, 31, v4
	s_waitcnt lgkmcnt(3)
	v_ashrrev_i32_e32 v7, 31, v6
	s_waitcnt lgkmcnt(2)
	v_ashrrev_i32_e32 v11, 31, v10
	s_waitcnt lgkmcnt(1)
	v_ashrrev_i32_e32 v1, 31, v0
	v_lshlrev_b64 v[0:1], 7, v[0:1]
	v_lshl_add_u64 v[0:1], v[30:31], 0, v[0:1]
	global_load_dwordx4 v[16:19], v[0:1], off
	v_lshlrev_b64 v[0:1], 7, v[4:5]
	s_waitcnt lgkmcnt(0)
	v_ashrrev_i32_e32 v3, 31, v2
	v_lshl_add_u64 v[0:1], v[30:31], 0, v[0:1]
	global_load_dwordx4 v[20:23], v[0:1], off
	v_lshlrev_b64 v[0:1], 7, v[2:3]
	v_lshl_add_u64 v[0:1], v[30:31], 0, v[0:1]
	global_load_dwordx4 v[12:15], v[0:1], off
	v_lshlrev_b64 v[0:1], 7, v[6:7]
	v_lshl_add_u64 v[0:1], v[30:31], 0, v[0:1]
	global_load_dwordx4 v[4:7], v[0:1], off
	ds_bpermute_b32 v0, v47, v8 offset:240
	v_lshlrev_b64 v[2:3], 7, v[10:11]
	v_lshl_add_u64 v[2:3], v[30:31], 0, v[2:3]
	global_load_dwordx4 v[8:11], v[2:3], off
	ds_bpermute_b32 v46, v47, v49 offset:128
	s_waitcnt lgkmcnt(1)
	v_ashrrev_i32_e32 v1, 31, v0
	v_lshlrev_b64 v[0:1], 7, v[0:1]
	v_lshl_add_u64 v[0:1], v[30:31], 0, v[0:1]
	global_load_dwordx4 v[0:3], v[0:1], off
	ds_bpermute_b32 v48, v47, v49 offset:144
	ds_bpermute_b32 v50, v47, v49 offset:160
	ds_bpermute_b32 v44, v47, v49 offset:176
	ds_bpermute_b32 v40, v47, v49 offset:192
	ds_bpermute_b32 v42, v47, v49 offset:208
	s_waitcnt vmcnt(7)
	s_waitcnt vmcnt(6)
	s_waitcnt vmcnt(5)
	s_waitcnt lgkmcnt(5)
	v_fma_mix_f32 v36, v46, v52, v36 op_sel_hi:[0,1,0]
	v_fma_mix_f32 v37, v46, v52, v37 op_sel:[0,1,0] op_sel_hi:[0,1,0]
	s_waitcnt vmcnt(4)
	v_fma_mix_f32 v38, v46, v53, v38 op_sel_hi:[0,1,0]
	v_fma_mix_f32 v39, v46, v53, v39 op_sel:[0,1,0] op_sel_hi:[0,1,0]
	s_waitcnt vmcnt(3)
	v_cvt_f32_f16_e32 v56, v54
	v_cvt_f32_f16_sdwa v57, v54 dst_sel:DWORD dst_unused:UNUSED_PAD src0_sel:WORD_1
	ds_bpermute_b32 v54, v47, v49 offset:224
	s_waitcnt lgkmcnt(5)
	v_fma_mix_f32 v36, v48, v58, v36 op_sel_hi:[0,1,0]
	v_fma_mix_f32 v37, v48, v58, v37 op_sel:[0,1,0] op_sel_hi:[0,1,0]
	s_waitcnt vmcnt(2)
	v_fma_mix_f32 v38, v48, v59, v38 op_sel_hi:[0,1,0]
	v_fma_mix_f32 v39, v48, v59, v39 op_sel:[0,1,0] op_sel_hi:[0,1,0]
	ds_bpermute_b32 v52, v47, v49 offset:240
	s_waitcnt lgkmcnt(5)
	v_fma_mix_f32 v36, v50, v16, v36 op_sel_hi:[0,1,0]
	v_fma_mix_f32 v37, v50, v16, v37 op_sel:[0,1,0] op_sel_hi:[0,1,0]
	s_waitcnt vmcnt(1)
	v_fma_mix_f32 v16, v50, v17, v38 op_sel_hi:[0,1,0]
	v_fma_mix_f32 v17, v50, v17, v39 op_sel:[0,1,0] op_sel_hi:[0,1,0]
	s_waitcnt lgkmcnt(4)
	v_fma_mix_f32 v36, v44, v20, v36 op_sel_hi:[0,1,0]
	v_fma_mix_f32 v37, v44, v20, v37 op_sel:[0,1,0] op_sel_hi:[0,1,0]
	s_waitcnt vmcnt(0)
	v_fma_mix_f32 v16, v44, v21, v16 op_sel_hi:[0,1,0]
	v_fma_mix_f32 v17, v44, v21, v17 op_sel:[0,1,0] op_sel_hi:[0,1,0]
	s_waitcnt lgkmcnt(3)
	v_fma_mix_f32 v20, v40, v12, v36 op_sel_hi:[0,1,0]
	v_fma_mix_f32 v21, v40, v12, v37 op_sel:[0,1,0] op_sel_hi:[0,1,0]
	v_fma_mix_f32 v12, v40, v13, v16 op_sel_hi:[0,1,0]
	v_fma_mix_f32 v13, v40, v13, v17 op_sel:[0,1,0] op_sel_hi:[0,1,0]
	s_waitcnt lgkmcnt(2)
	v_fma_mix_f32 v20, v42, v4, v20 op_sel_hi:[0,1,0]
	v_fma_mix_f32 v21, v42, v4, v21 op_sel:[0,1,0] op_sel_hi:[0,1,0]
	v_fma_mix_f32 v4, v42, v5, v12 op_sel_hi:[0,1,0]
	v_fma_mix_f32 v5, v42, v5, v13 op_sel:[0,1,0] op_sel_hi:[0,1,0]
	s_waitcnt lgkmcnt(1)
	v_fma_mix_f32 v20, v54, v8, v20 op_sel_hi:[0,1,0]
	v_fma_mix_f32 v21, v54, v8, v21 op_sel:[0,1,0] op_sel_hi:[0,1,0]
	v_fma_mix_f32 v4, v54, v9, v4 op_sel_hi:[0,1,0]
	v_fma_mix_f32 v5, v54, v9, v5 op_sel:[0,1,0] op_sel_hi:[0,1,0]
	s_waitcnt lgkmcnt(0)
	v_fma_mix_f32 v36, v52, v0, v20 op_sel_hi:[0,1,0]
	v_fma_mix_f32 v37, v52, v0, v21 op_sel:[0,1,0] op_sel_hi:[0,1,0]
	v_fma_mix_f32 v38, v52, v1, v4 op_sel_hi:[0,1,0]
	v_fma_mix_f32 v39, v52, v1, v5 op_sel:[0,1,0] op_sel_hi:[0,1,0]
	v_pk_fma_f32 v[8:9], v[46:47], v[56:57], v[32:33] op_sel_hi:[0,1,1]
	v_fma_mix_f32 v8, v48, v60, v8 op_sel_hi:[0,1,0]
	v_fma_mix_f32 v9, v48, v60, v9 op_sel:[0,1,0] op_sel_hi:[0,1,0]
	v_fma_mix_f32 v0, v50, v18, v8 op_sel_hi:[0,1,0]
	v_fma_mix_f32 v1, v50, v18, v9 op_sel:[0,1,0] op_sel_hi:[0,1,0]
	v_fma_mix_f32 v0, v44, v22, v0 op_sel_hi:[0,1,0]
	v_fma_mix_f32 v1, v44, v22, v1 op_sel:[0,1,0] op_sel_hi:[0,1,0]
	v_fma_mix_f32 v0, v40, v14, v0 op_sel_hi:[0,1,0]
	v_fma_mix_f32 v1, v40, v14, v1 op_sel:[0,1,0] op_sel_hi:[0,1,0]
	v_fma_mix_f32 v0, v42, v6, v0 op_sel_hi:[0,1,0]
	v_fma_mix_f32 v1, v42, v6, v1 op_sel:[0,1,0] op_sel_hi:[0,1,0]
	v_fma_mix_f32 v0, v54, v10, v0 op_sel_hi:[0,1,0]
	v_fma_mix_f32 v1, v54, v10, v1 op_sel:[0,1,0] op_sel_hi:[0,1,0]
	v_fma_mix_f32 v32, v52, v2, v0 op_sel_hi:[0,1,0]
	v_fma_mix_f32 v33, v52, v2, v1 op_sel:[0,1,0] op_sel_hi:[0,1,0]
	v_fma_mix_f32 v8, v46, v55, v34 op_sel_hi:[0,1,0]
	v_fma_mix_f32 v9, v46, v55, v35 op_sel:[0,1,0] op_sel_hi:[0,1,0]
	v_fma_mix_f32 v8, v48, v61, v8 op_sel_hi:[0,1,0]
	v_fma_mix_f32 v9, v48, v61, v9 op_sel:[0,1,0] op_sel_hi:[0,1,0]
	v_fma_mix_f32 v0, v50, v19, v8 op_sel_hi:[0,1,0]
	v_fma_mix_f32 v1, v50, v19, v9 op_sel:[0,1,0] op_sel_hi:[0,1,0]
	v_fma_mix_f32 v0, v44, v23, v0 op_sel_hi:[0,1,0]
	v_fma_mix_f32 v1, v44, v23, v1 op_sel:[0,1,0] op_sel_hi:[0,1,0]
	v_fma_mix_f32 v0, v40, v15, v0 op_sel_hi:[0,1,0]
	v_fma_mix_f32 v1, v40, v15, v1 op_sel:[0,1,0] op_sel_hi:[0,1,0]
	v_fma_mix_f32 v0, v42, v7, v0 op_sel_hi:[0,1,0]
	v_fma_mix_f32 v1, v42, v7, v1 op_sel:[0,1,0] op_sel_hi:[0,1,0]
	v_fma_mix_f32 v0, v54, v11, v0 op_sel_hi:[0,1,0]
	v_fma_mix_f32 v1, v54, v11, v1 op_sel:[0,1,0] op_sel_hi:[0,1,0]
	v_fma_mix_f32 v34, v52, v3, v0 op_sel_hi:[0,1,0]
	v_fma_mix_f32 v35, v52, v3, v1 op_sel:[0,1,0] op_sel_hi:[0,1,0]

	.amdhsa_kernel _Z6k_agg2PKDv4_jPKiS3_PK15HIP_vector_typeIiLj2EEPKfPfSA_PS_
		.amdhsa_group_segment_fixed_size 0
		.amdhsa_private_segment_fixed_size 0
		.amdhsa_kernarg_size 64
		.amdhsa_user_sgpr_count 2
		.amdhsa_user_sgpr_dispatch_ptr 0
		.amdhsa_user_sgpr_queue_ptr 0
		.amdhsa_user_sgpr_kernarg_segment_ptr 1
		.amdhsa_user_sgpr_dispatch_id 0
		.amdhsa_user_sgpr_kernarg_preload_length 0
		.amdhsa_user_sgpr_kernarg_preload_offset 0
		.amdhsa_user_sgpr_private_segment_size 0
		.amdhsa_uses_dynamic_stack 0
		.amdhsa_enable_private_segment 0
		.amdhsa_system_sgpr_workgroup_id_x 1
		.amdhsa_system_sgpr_workgroup_id_y 0
		.amdhsa_system_sgpr_workgroup_id_z 0
		.amdhsa_system_sgpr_workgroup_info 0
		.amdhsa_system_vgpr_workitem_id 0
		.amdhsa_next_free_vgpr 62
		.amdhsa_next_free_sgpr 12
		.amdhsa_accum_offset 64
		.amdhsa_reserve_vcc 1
		.amdhsa_float_round_mode_32 0
		.amdhsa_float_round_mode_16_64 0
		.amdhsa_float_denorm_mode_32 3
		.amdhsa_float_denorm_mode_16_64 3
		.amdhsa_dx10_clamp 1
		.amdhsa_ieee_mode 1
		.amdhsa_fp16_overflow 0
		.amdhsa_tg_split 0
		.amdhsa_exception_fp_ieee_invalid_op 0
		.amdhsa_exception_fp_denorm_src 0
		.amdhsa_exception_fp_ieee_div_zero 0
		.amdhsa_exception_fp_ieee_overflow 0
		.amdhsa_exception_fp_ieee_underflow 0
		.amdhsa_exception_fp_ieee_inexact 0
		.amdhsa_exception_int_div_zero 0
	.end_amdhsa_kernel

amdhsa.kernels:
  - .agpr_count:     0
    .args:
      - .actual_access:  read_only
        .address_space:  global
        .offset:         0
        .size:           8
        .value_kind:     global_buffer
      - .actual_access:  read_only
        .address_space:  global
        .offset:         8
        .size:           8
        .value_kind:     global_buffer
      - .actual_access:  read_only
        .address_space:  global
        .offset:         16
        .size:           8
        .value_kind:     global_buffer
      - .actual_access:  write_only
        .address_space:  global
        .offset:         24
        .size:           8
        .value_kind:     global_buffer
      - .actual_access:  write_only
        .address_space:  global
        .offset:         32
        .size:           8
        .value_kind:     global_buffer
      - .actual_access:  write_only
        .address_space:  global
        .offset:         40
        .size:           8
        .value_kind:     global_buffer
      - .actual_access:  read_only
        .address_space:  global
        .offset:         48
        .size:           8
        .value_kind:     global_buffer
      - .actual_access:  read_only
        .address_space:  global
        .offset:         56
        .size:           8
        .value_kind:     global_buffer
      - .actual_access:  read_only
        .address_space:  global
        .offset:         64
        .size:           8
        .value_kind:     global_buffer
      - .actual_access:  write_only
        .address_space:  global
        .offset:         72
        .size:           8
        .value_kind:     global_buffer
    .group_segment_fixed_size: 0
    .kernarg_segment_align: 8
    .kernarg_segment_size: 80
    .language:       OpenCL C
    .language_version:
      - 2
      - 0
    .max_flat_workgroup_size: 256
    .name:           _Z8k_phase1PKfS0_S0_PDv4_jS2_PiS3_P15HIP_vector_typeIiLj2EES0_Pf
    .private_segment_fixed_size: 0
    .sgpr_count:     18
    .sgpr_spill_count: 0
    .symbol:         _Z8k_phase1PKfS0_S0_PDv4_jS2_PiS3_P15HIP_vector_typeIiLj2EES0_Pf.kd
    .uniform_work_group_size: 1
    .uses_dynamic_stack: false
    .vgpr_count:     19
    .vgpr_spill_count: 0
    .wavefront_size: 64
  - .agpr_count:     0
    .args:
      - .actual_access:  read_only
        .address_space:  global
        .offset:         0
        .size:           8
        .value_kind:     global_buffer
      - .actual_access:  read_only
        .address_space:  global
        .offset:         8
        .size:           8
        .value_kind:     global_buffer
      - .actual_access:  read_only
        .address_space:  global
        .offset:         16
        .size:           8
        .value_kind:     global_buffer
      - .actual_access:  read_only
        .address_space:  global
        .offset:         24
        .size:           8
        .value_kind:     global_buffer
      - .address_space:  global
        .offset:         32
        .size:           8
        .value_kind:     global_buffer
      - .actual_access:  write_only
        .address_space:  global
        .offset:         40
        .size:           8
        .value_kind:     global_buffer
      - .actual_access:  write_only
        .address_space:  global
        .offset:         48
        .size:           8
        .value_kind:     global_buffer
      - .actual_access:  write_only
        .address_space:  global
        .offset:         56
        .size:           8
        .value_kind:     global_buffer
      - .actual_access:  read_only
        .address_space:  global
        .offset:         64
        .size:           8
        .value_kind:     global_buffer
      - .actual_access:  write_only
        .address_space:  global
        .offset:         72
        .size:           8
        .value_kind:     global_buffer
      - .actual_access:  write_only
        .address_space:  global
        .offset:         80
        .size:           8
        .value_kind:     global_buffer
    .group_segment_fixed_size: 90112
    .kernarg_segment_align: 8
    .kernarg_segment_size: 88
    .language:       OpenCL C
    .language_version:
      - 2
      - 0
    .max_flat_workgroup_size: 768
    .name:           _Z7k_gemm1PKfS0_PKDv4_jPKiPiS6_P15HIP_vector_typeIiLj2EEPDF16_S0_S6_S9_
    .private_segment_fixed_size: 0
    .sgpr_count:     48
    .sgpr_spill_count: 0
    .symbol:         _Z7k_gemm1PKfS0_PKDv4_jPKiPiS6_P15HIP_vector_typeIiLj2EEPDF16_S0_S6_S9_.kd
    .uniform_work_group_size: 1
    .uses_dynamic_stack: false
    .vgpr_count:     168
    .vgpr_spill_count: 0
    .wavefront_size: 64
  - .agpr_count:     0
    .args:
      - .actual_access:  read_only
        .address_space:  global
        .offset:         0
        .size:           8
        .value_kind:     global_buffer
      - .actual_access:  read_only
        .address_space:  global
        .offset:         8
        .size:           8
        .value_kind:     global_buffer
      - .actual_access:  read_only
        .address_space:  global
        .offset:         16
        .size:           8
        .value_kind:     global_buffer
      - .actual_access:  read_only
        .address_space:  global
        .offset:         24
        .size:           8
        .value_kind:     global_buffer
      - .actual_access:  read_only
        .address_space:  global
        .offset:         32
        .size:           8
        .value_kind:     global_buffer
      - .actual_access:  read_only
        .address_space:  global
        .offset:         40
        .size:           8
        .value_kind:     global_buffer
      - .actual_access:  write_only
        .address_space:  global
        .offset:         48
        .size:           8
        .value_kind:     global_buffer
    .group_segment_fixed_size: 12576
    .kernarg_segment_align: 8
    .kernarg_segment_size: 56
    .language:       OpenCL C
    .language_version:
      - 2
      - 0
    .max_flat_workgroup_size: 256
    .name:           _Z8k_agg1g2PKDv4_jPKiS3_PK15HIP_vector_typeIiLj2EEPKfS1_PDF16_
    .private_segment_fixed_size: 0
    .sgpr_count:     52
    .sgpr_spill_count: 0
    .symbol:         _Z8k_agg1g2PKDv4_jPKiS3_PK15HIP_vector_typeIiLj2EEPKfS1_PDF16_.kd
    .uniform_work_group_size: 1
    .uses_dynamic_stack: false
    .vgpr_count:     126
    .vgpr_spill_count: 0
    .wavefront_size: 64
  - .agpr_count:     0
    .args:
      - .actual_access:  read_only
        .address_space:  global
        .offset:         0
        .size:           8
        .value_kind:     global_buffer
      - .actual_access:  read_only
        .address_space:  global
        .offset:         8
        .size:           8
        .value_kind:     global_buffer
      - .actual_access:  read_only
        .address_space:  global
        .offset:         16
        .size:           8
        .value_kind:     global_buffer
      - .actual_access:  read_only
        .address_space:  global
        .offset:         24
        .size:           8
        .value_kind:     global_buffer
      - .actual_access:  read_only
        .address_space:  global
        .offset:         32
        .size:           8
        .value_kind:     global_buffer
      - .actual_access:  write_only
        .address_space:  global
        .offset:         40
        .size:           8
        .value_kind:     global_buffer
      - .actual_access:  write_only
        .address_space:  global
        .offset:         48
        .size:           8
        .value_kind:     global_buffer
      - .actual_access:  write_only
        .address_space:  global
        .offset:         56
        .size:           8
        .value_kind:     global_buffer
    .group_segment_fixed_size: 0
    .kernarg_segment_align: 8
    .kernarg_segment_size: 64
    .language:       OpenCL C
    .language_version:
      - 2
      - 0
    .max_flat_workgroup_size: 256
    .name:           _Z6k_agg2PKDv4_jPKiS3_PK15HIP_vector_typeIiLj2EEPKfPfSA_PS_
    .private_segment_fixed_size: 0
    .sgpr_count:     18
    .sgpr_spill_count: 0
    .symbol:         _Z6k_agg2PKDv4_jPKiS3_PK15HIP_vector_typeIiLj2EEPKfPfSA_PS_.kd
    .uniform_work_group_size: 1
    .uses_dynamic_stack: false
    .vgpr_count:     62
    .vgpr_spill_count: 0
    .wavefront_size: 64
  - .agpr_count:     0
    .args:
      - .actual_access:  read_only
        .address_space:  global
        .offset:         0
        .size:           8
        .value_kind:     global_buffer
      - .actual_access:  read_only
        .address_space:  global
        .offset:         8
        .size:           8
        .value_kind:     global_buffer
      - .actual_access:  read_only
        .address_space:  global
        .offset:         16
        .size:           8
        .value_kind:     global_buffer
      - .actual_access:  read_only
        .address_space:  global
        .offset:         24
        .size:           8
        .value_kind:     global_buffer
      - .actual_access:  read_only
        .address_space:  global
        .offset:         32
        .size:           8
        .value_kind:     global_buffer
      - .actual_access:  read_only
        .address_space:  global
        .offset:         40
        .size:           8
        .value_kind:     global_buffer
      - .actual_access:  read_only
        .address_space:  global
        .offset:         48
        .size:           8
        .value_kind:     global_buffer
      - .actual_access:  write_only
        .address_space:  global
        .offset:         56
        .size:           8
        .value_kind:     global_buffer
      - .actual_access:  write_only
        .address_space:  global
        .offset:         64
        .size:           8
        .value_kind:     global_buffer
    .group_segment_fixed_size: 6144
    .kernarg_segment_align: 8
    .kernarg_segment_size: 72
    .language:       OpenCL C
    .language_version:
      - 2
      - 0
    .max_flat_workgroup_size: 256
    .name:           _Z9k_readoutPKDv4_jPKfPKiPK15HIP_vector_typeIiLj2EES3_S3_S3_PfSA_
    .private_segment_fixed_size: 0
    .sgpr_count:     20
    .sgpr_spill_count: 0
    .symbol:         _Z9k_readoutPKDv4_jPKfPKiPK15HIP_vector_typeIiLj2EES3_S3_S3_PfSA_.kd
    .uniform_work_group_size: 1
    .uses_dynamic_stack: false
    .vgpr_count:     92
    .vgpr_spill_count: 0
    .wavefront_size: 64
